# Fourier stage A unit loop: the DFT-matrix and twiddle loads of a unit are issued right after the staging barrier, ahead of the next unit's tile prefetch, and consumed with counted waits that leave the
# speedup vs baseline: 1.0034x; 1.0034x over previous
;     __device__ __forceinline__ float* tw() const { return (float*)(ws + WS_TW); }
;     __device__ __forceinline__ bf16_t* zm() const { return (bf16_t*)(ws + WS_ZM); }
; __device__ __forceinline__ int v_rd_base(int lane) { return ((lane & 3) << 3) | (((lane >> 2) & 3) << 6) | (((lane >> 4) & 1) << 5) | (((lane >> 5) & 1) << 8); }
; __device__ __forceinline__ void phase_fft_a(const Frame& F) {
;     ...
;         f32x16 zc[2] = {f32x16{}, f32x16{}}, zs[2] = {f32x16{}, f32x16{}};
; #pragma unroll
;         for (int t = 0; t < 2; ++t) {
;             bf16x8 bc[4], bs[4];
; #pragma unroll
;             for (int ks = 0; ks < 4; ++ks) { const int o = k1 * 128 + t * 64 + ks * 16 + hi * 8; bc[ks] = *(const bf16x8*)(dc + o); bs[ks] = *(const bf16x8*)(ds + o); }
;             const int vb = (int)(uintptr_t)img + t * 16384 + ff::v_rd_base(lane) + chh * 1024;
;             ff::xt_two<0>(zc[0], zs[0], vb, bc, bs);
;             ff::xt_two<1>(zc[1], zs[1], vb, bc, bs);
;         }
;         const f32x2 t2 = *(const f32x2*)(F.tw() + (size_t)(k1 * 64 + n2) * 2);
;         bf16_t* zp = F.zm() + (size_t)((b * 128 + k1) * 64 + n2) * DM + cb * 128 + 64 * chh + 4 * hi;
.LBB0_326:
	v_add_u32_e32 v115, s30, v123
	ds_read_b64_tr_b16 v[6:7], v115 offset:0
	ds_read_b64_tr_b16 v[8:9], v115 offset:0x800
	ds_read_b64_tr_b16 v[10:11], v115 offset:0x1000
	ds_read_b64_tr_b16 v[12:13], v115 offset:0x1800
	ds_read_b64_tr_b16 v[14:15], v115 offset:0x2000
	ds_read_b64_tr_b16 v[16:17], v115 offset:0x2800
	ds_read_b64_tr_b16 v[22:23], v115 offset:0x3000
	ds_read_b64_tr_b16 v[24:25], v115 offset:0x3800
	s_waitcnt lgkmcnt(0)
	s_bfe_u32 s8, s23, 0x60002
	s_waitcnt vmcnt(20)
	v_mfma_f32_32x32x16_bf16 v[34:49], v[6:9], v[2:5], 0
	s_waitcnt vmcnt(19)
	v_mfma_f32_32x32x16_bf16 v[50:65], v[6:9], v[18:21], 0
	s_waitcnt vmcnt(18)
	v_mfma_f32_32x32x16_bf16 v[34:49], v[10:13], v[116:119], v[34:49]
	s_waitcnt vmcnt(17)
	v_mfma_f32_32x32x16_bf16 v[50:65], v[10:13], v[128:131], v[50:65]
	s_waitcnt vmcnt(16)
	v_mfma_f32_32x32x16_bf16 v[34:49], v[14:17], v[132:135], v[34:49]
	s_waitcnt vmcnt(15)
	v_mfma_f32_32x32x16_bf16 v[50:65], v[14:17], v[136:139], v[50:65]
	s_waitcnt vmcnt(14)
	v_mfma_f32_32x32x16_bf16 v[34:49], v[22:25], v[140:143], v[34:49]
	s_waitcnt vmcnt(13)
	v_mfma_f32_32x32x16_bf16 v[50:65], v[22:25], v[148:151], v[50:65]
	ds_read_b64_tr_b16 v[22:23], v115 offset:0x200
	ds_read_b64_tr_b16 v[24:25], v115 offset:0xa00
	ds_read_b64_tr_b16 v[152:153], v115 offset:0x1200
	ds_read_b64_tr_b16 v[154:155], v115 offset:0x1a00
	ds_read_b64_tr_b16 v[156:157], v115 offset:0x2200
	ds_read_b64_tr_b16 v[158:159], v115 offset:0x2a00
	ds_read_b64_tr_b16 v[160:161], v115 offset:0x3200
	ds_read_b64_tr_b16 v[162:163], v115 offset:0x3a00
	s_waitcnt lgkmcnt(0)
	s_nop 0
	v_mfma_f32_32x32x16_bf16 v[2:17], v[22:25], v[2:5], 0
	v_add_u32_e32 v115, 0x4000, v115
	v_mfma_f32_32x32x16_bf16 v[18:33], v[22:25], v[18:21], 0
	v_mfma_f32_32x32x16_bf16 v[2:17], v[152:155], v[116:119], v[2:17]
	v_mfma_f32_32x32x16_bf16 v[18:33], v[152:155], v[128:131], v[18:33]
	v_mfma_f32_32x32x16_bf16 v[2:17], v[156:159], v[132:135], v[2:17]
	v_mfma_f32_32x32x16_bf16 v[18:33], v[156:159], v[136:139], v[18:33]
	v_mfma_f32_32x32x16_bf16 v[2:17], v[160:163], v[140:143], v[2:17]
	v_mfma_f32_32x32x16_bf16 v[18:33], v[160:163], v[148:151], v[18:33]
	ds_read_b64_tr_b16 v[160:161], v115 offset:0
	ds_read_b64_tr_b16 v[162:163], v115 offset:0x800
	ds_read_b64_tr_b16 v[164:165], v115 offset:0x1000
	ds_read_b64_tr_b16 v[166:167], v115 offset:0x1800
	ds_read_b64_tr_b16 v[168:169], v115 offset:0x2000
	ds_read_b64_tr_b16 v[170:171], v115 offset:0x2800
	ds_read_b64_tr_b16 v[172:173], v115 offset:0x3000
	ds_read_b64_tr_b16 v[174:175], v115 offset:0x3800
	s_waitcnt lgkmcnt(0)
	s_waitcnt vmcnt(12)
	v_mfma_f32_32x32x16_bf16 v[34:49], v[160:163], v[184:187], v[34:49]
	s_waitcnt vmcnt(11)
	v_mfma_f32_32x32x16_bf16 v[50:65], v[160:163], v[188:191], v[50:65]
	ds_read_b64_tr_b16 v[160:161], v115 offset:0x200
	ds_read_b64_tr_b16 v[162:163], v115 offset:0xa00
	s_waitcnt vmcnt(10)
	v_mfma_f32_32x32x16_bf16 v[34:49], v[164:167], v[192:195], v[34:49]
	s_waitcnt vmcnt(9)
	v_mfma_f32_32x32x16_bf16 v[50:65], v[164:167], v[198:201], v[50:65]
	ds_read_b64_tr_b16 v[164:165], v115 offset:0x1200
	ds_read_b64_tr_b16 v[166:167], v115 offset:0x1a00
	s_waitcnt vmcnt(8)
	v_mfma_f32_32x32x16_bf16 v[34:49], v[168:171], v[202:205], v[34:49]
	s_waitcnt vmcnt(7)
	v_mfma_f32_32x32x16_bf16 v[50:65], v[168:171], v[206:209], v[50:65]
	ds_read_b64_tr_b16 v[168:169], v115 offset:0x2200
	ds_read_b64_tr_b16 v[170:171], v115 offset:0x2a00
	s_waitcnt vmcnt(6)
	v_mfma_f32_32x32x16_bf16 v[34:49], v[172:175], v[210:213], v[34:49]
	s_waitcnt vmcnt(5)
	v_mfma_f32_32x32x16_bf16 v[50:65], v[172:175], v[214:217], v[50:65]
	ds_read_b64_tr_b16 v[172:173], v115 offset:0x3200
	ds_read_b64_tr_b16 v[174:175], v115 offset:0x3a00
	s_waitcnt lgkmcnt(0)
	v_lshl_or_b32 v115, s8, 3, v126
	v_mfma_f32_32x32x16_bf16 v[2:17], v[160:163], v[184:187], v[2:17]
	s_lshr_b32 s9, s23, 1
	s_and_b32 s9, s9, 0x3ffff80
	v_or_b32_e32 v115, s9, v120
	v_lshl_or_b32 v118, v115, 6, s8
	v_ashrrev_i32_e32 v119, 31, v118
	s_and_b32 s22, s22, 0x180
	v_mfma_f32_32x32x16_bf16 v[18:33], v[160:163], v[188:191], v[18:33]
	v_lshlrev_b64 v[118:119], 11, v[118:119]
	v_mov_b32_e32 v128, v34
	v_mov_b32_e32 v129, v50
	v_mov_b32_e32 v130, v50
	v_mov_b32_e32 v131, v34
	v_mov_b32_e32 v50, v35
	v_mov_b32_e32 v34, v51
	v_mfma_f32_32x32x16_bf16 v[2:17], v[164:167], v[192:195], v[2:17]
	v_mov_b32_e32 v132, v36
	v_mov_b32_e32 v133, v52
	s_lshl_b32 s76, s22, 1
	v_lshl_add_u64 v[118:119], s[24:25], 0, v[118:119]
	v_mov_b32_e32 v134, v52
	v_mov_b32_e32 v135, v36
	v_mov_b32_e32 v52, v37
	v_mov_b32_e32 v36, v53
	v_lshl_add_u64 v[118:119], v[118:119], 0, s[76:77]
	v_mfma_f32_32x32x16_bf16 v[18:33], v[164:167], v[198:201], v[18:33]
	v_mov_b32_e32 v136, v38
	v_mov_b32_e32 v137, v54
	v_mov_b32_e32 v138, v54
	v_mov_b32_e32 v139, v38
	v_mov_b32_e32 v54, v39
	v_mov_b32_e32 v38, v55
	v_lshl_add_u64 v[118:119], s[28:29], 1, v[118:119]
	v_mfma_f32_32x32x16_bf16 v[2:17], v[168:171], v[202:205], v[2:17]
	v_mov_b32_e32 v140, v40
	v_mov_b32_e32 v141, v56
	v_mov_b32_e32 v142, v56
	v_mov_b32_e32 v56, v41
	v_mov_b32_e32 v143, v40
	v_mov_b32_e32 v40, v57
	v_lshl_add_u64 v[118:119], v[118:119], 0, v[146:147]
	v_mfma_f32_32x32x16_bf16 v[18:33], v[168:171], v[206:209], v[18:33]
	s_xor_b32 s0, s0, 1
	s_add_i32 s1, s1, s31
	s_andn2_b64 vcc, exec, s[18:19]
	s_mov_b32 s22, s7
	s_mov_b32 s23, s2
	s_waitcnt vmcnt(4)
; __device__ __forceinline__ unsigned cvt_pk_bf16(float lo, float hi) { unsigned r; asm volatile("v_cvt_pk_bf16_f32 %0, %1, %2" : "=v"(r) : "v"(lo), "v"(hi)); return r; }
; __device__ __forceinline__ void phase_fft_a(const Frame& F) {
;     ...
; #pragma unroll
;         for (int dd = 0; dd < 2; ++dd)
; #pragma unroll
;             for (int g = 0; g < 4; ++g) {
;                 float p[4], q[4];
; #pragma unroll
;                 for (int j = 0; j < 4; ++j) { const float c = zc[dd][4 * g + j], s = zs[dd][4 * g + j]; p[j] = c * t2.x - s * t2.y; q[j] = c * t2.y + s * t2.x; }
;                 u32x2 wp, wq; wp.x = cvt_pk_bf16(p[0], p[1]); wp.y = cvt_pk_bf16(p[2], p[3]); wq.x = cvt_pk_bf16(q[0], q[1]); wq.y = cvt_pk_bf16(q[2], q[3]);
;                 *(u32x2*)(zp + dd * 32 + 8 * g) = wp; *(u32x2*)(zp + 512 + dd * 32 + 8 * g) = wq;
	v_pk_mul_f32 v[50:51], v[50:51], v[218:219]
	v_pk_mul_f32 v[34:35], v[34:35], v[218:219]
	v_pk_mul_f32 v[132:133], v[132:133], v[218:219]
	v_pk_mul_f32 v[128:129], v[128:129], v[218:219]
	v_pk_mul_f32 v[52:53], v[52:53], v[218:219]
	v_pk_mul_f32 v[36:37], v[36:37], v[218:219]
	v_sub_f32_e32 v50, v50, v51
	v_add_f32_e32 v51, v35, v34
	v_sub_f32_e32 v35, v132, v133
	v_pk_mul_f32 v[130:131], v[130:131], v[218:219]
	v_pk_mul_f32 v[134:135], v[134:135], v[218:219]
	v_pk_mul_f32 v[136:137], v[136:137], v[218:219]
	v_pk_mul_f32 v[54:55], v[54:55], v[218:219]
	v_pk_mul_f32 v[38:39], v[38:39], v[218:219]
	v_pk_mul_f32 v[140:141], v[140:141], v[218:219]
	v_pk_mul_f32 v[56:57], v[56:57], v[218:219]
	v_sub_f32_e32 v115, v128, v129
	v_sub_f32_e32 v52, v52, v53
	v_add_f32_e32 v37, v37, v36
	v_cvt_pk_bf16_f32 v34, v115, v50
	v_cvt_pk_bf16_f32 v35, v35, v52
	v_pk_mul_f32 v[138:139], v[138:139], v[218:219]
	v_pk_mul_f32 v[142:143], v[142:143], v[218:219]
	v_pk_mul_f32 v[40:41], v[40:41], v[218:219]
	v_add_f32_e32 v127, v131, v130
	v_add_f32_e32 v128, v135, v134
	v_sub_f32_e32 v53, v136, v137
	v_sub_f32_e32 v54, v54, v55
	v_add_f32_e32 v38, v39, v38
	v_sub_f32_e32 v39, v140, v141
	v_sub_f32_e32 v56, v56, v57
	v_cvt_pk_bf16_f32 v36, v127, v51
	v_cvt_pk_bf16_f32 v37, v128, v37
	ds_write_b64 v176, v[34:35]
	ds_write_b64 v176, v[36:37] offset:128
	v_cvt_pk_bf16_f32 v34, v53, v54
	v_cvt_pk_bf16_f32 v35, v39, v56
	v_add_f32_e32 v129, v139, v138
	v_add_f32_e32 v55, v143, v142
	v_add_f32_e32 v40, v41, v40
	v_cvt_pk_bf16_f32 v36, v129, v38
	v_cvt_pk_bf16_f32 v37, v55, v40
	ds_write_b64 v176, v[34:35] offset:16
	ds_write_b64 v176, v[36:37] offset:144
	v_mov_b32_e32 v34, v42
	v_mov_b32_e32 v35, v58
	v_pk_mul_f32 v[34:35], v[34:35], v[218:219]
	v_mfma_f32_32x32x16_bf16 v[2:17], v[172:175], v[210:213], v[2:17]
	v_sub_f32_e32 v36, v34, v35
	v_mov_b32_e32 v34, v58
	v_mov_b32_e32 v35, v42
	v_mul_f32_e64 v34, v34, v218
	v_mul_f32_e64 v35, v35, v219
	v_mov_b32_e32 v58, v43
	v_add_f32_e32 v37, v35, v34
	v_pk_mul_f32 v[34:35], v[58:59], v[218:219]
	v_mov_b32_e32 v42, v59
	v_sub_f32_e32 v38, v34, v35
	v_pk_mul_f32 v[34:35], v[42:43], v[218:219]
	v_mfma_f32_32x32x16_bf16 v[18:33], v[172:175], v[214:217], v[18:33]
	v_add_f32_e32 v39, v35, v34
	v_mov_b32_e32 v34, v44
	v_mov_b32_e32 v35, v60
	v_mul_f32_e64 v34, v34, v218
	v_mul_f32_e64 v35, v35, v219
	v_sub_f32_e32 v40, v34, v35
	v_mov_b32_e32 v34, v60
	v_mov_b32_e32 v35, v44
	v_pk_mul_f32 v[34:35], v[34:35], v[218:219]
	v_mov_b32_e32 v60, v45
	v_add_f32_e32 v41, v35, v34
	v_pk_mul_f32 v[34:35], v[60:61], v[218:219]
	v_mov_b32_e32 v44, v61
	v_sub_f32_e32 v42, v34, v35
	v_pk_mul_f32 v[34:35], v[44:45], v[218:219]
	s_nop 0
	v_add_f32_e32 v43, v35, v34
	v_cvt_pk_bf16_f32 v34, v36, v38
	v_cvt_pk_bf16_f32 v35, v40, v42
	v_cvt_pk_bf16_f32 v36, v37, v39
	v_cvt_pk_bf16_f32 v37, v41, v43
	ds_write_b64 v176, v[34:35] offset:32
	ds_write_b64 v176, v[36:37] offset:160
	v_mov_b32_e32 v34, v46
	v_mov_b32_e32 v35, v62
	v_pk_mul_f32 v[34:35], v[34:35], v[218:219]
	s_nop 0
	v_sub_f32_e32 v36, v34, v35
	v_mov_b32_e32 v34, v62
	v_mov_b32_e32 v35, v46
	v_pk_mul_f32 v[34:35], v[34:35], v[218:219]
	v_mov_b32_e32 v62, v47
	v_add_f32_e32 v37, v35, v34
	v_pk_mul_f32 v[34:35], v[62:63], v[218:219]
	v_mov_b32_e32 v46, v63
	v_sub_f32_e32 v38, v34, v35
	v_pk_mul_f32 v[34:35], v[46:47], v[218:219]
	s_nop 0
	v_add_f32_e32 v39, v35, v34
	v_mov_b32_e32 v34, v48
	v_mov_b32_e32 v35, v64
	v_pk_mul_f32 v[34:35], v[34:35], v[218:219]
	s_nop 0
	v_sub_f32_e32 v40, v34, v35
	v_mov_b32_e32 v34, v64
	v_mov_b32_e32 v35, v48
	v_pk_mul_f32 v[34:35], v[34:35], v[218:219]
	v_mov_b32_e32 v64, v49
	v_add_f32_e32 v41, v35, v34
	v_pk_mul_f32 v[34:35], v[64:65], v[218:219]
	v_mov_b32_e32 v48, v65
	v_sub_f32_e32 v42, v34, v35
	v_pk_mul_f32 v[34:35], v[48:49], v[218:219]
	s_nop 0
	v_add_f32_e32 v43, v35, v34
	v_cvt_pk_bf16_f32 v34, v36, v38
	v_cvt_pk_bf16_f32 v35, v40, v42
	v_cvt_pk_bf16_f32 v36, v37, v39
	v_cvt_pk_bf16_f32 v37, v41, v43
	ds_write_b64 v176, v[34:35] offset:48
	ds_write_b64 v176, v[36:37] offset:176
	v_mov_b32_e32 v34, v2
	v_mov_b32_e32 v35, v18
	v_pk_mul_f32 v[34:35], v[34:35], v[218:219]
	s_nop 0
	v_sub_f32_e32 v36, v34, v35
	v_mov_b32_e32 v34, v18
	v_mov_b32_e32 v35, v2
	v_mov_b32_e32 v2, v19
	v_pk_mul_f32 v[34:35], v[34:35], v[218:219]
	v_mov_b32_e32 v18, v3
	v_pk_mul_f32 v[2:3], v[2:3], v[218:219]
	v_add_f32_e32 v37, v35, v34
	v_pk_mul_f32 v[34:35], v[18:19], v[218:219]
	v_add_f32_e32 v19, v3, v2
	v_mov_b32_e32 v2, v4
	v_mov_b32_e32 v3, v20
	v_pk_mul_f32 v[2:3], v[2:3], v[218:219]
	v_sub_f32_e32 v18, v34, v35
	v_sub_f32_e32 v34, v2, v3
	v_mov_b32_e32 v2, v20
	v_mov_b32_e32 v3, v4
	v_pk_mul_f32 v[2:3], v[2:3], v[218:219]
	v_mov_b32_e32 v20, v5
	v_add_f32_e32 v35, v3, v2
; __device__ __forceinline__ unsigned cvt_pk_bf16(float lo, float hi) { unsigned r; asm volatile("v_cvt_pk_bf16_f32 %0, %1, %2" : "=v"(r) : "v"(lo), "v"(hi)); return r; }
;     __device__ __forceinline__ float* tw() const { return (float*)(ws + WS_TW); }
;     __device__ __forceinline__ bf16_t* zm() const { return (bf16_t*)(ws + WS_ZM); }
; __device__ __forceinline__ void phase_fft_a(const Frame& F) {
;     ...
;         const f32x2 t2 = *(const f32x2*)(F.tw() + (size_t)(k1 * 64 + n2) * 2);
;         bf16_t* zp = F.zm() + (size_t)((b * 128 + k1) * 64 + n2) * DM + cb * 128 + 64 * chh + 4 * hi;
; #pragma unroll
;         for (int dd = 0; dd < 2; ++dd)
; #pragma unroll
;             for (int g = 0; g < 4; ++g) {
;                 float p[4], q[4];
; #pragma unroll
;                 for (int j = 0; j < 4; ++j) { const float c = zc[dd][4 * g + j], s = zs[dd][4 * g + j]; p[j] = c * t2.x - s * t2.y; q[j] = c * t2.y + s * t2.x; }
;                 u32x2 wp, wq; wp.x = cvt_pk_bf16(p[0], p[1]); wp.y = cvt_pk_bf16(p[2], p[3]); wq.x = cvt_pk_bf16(q[0], q[1]); wq.y = cvt_pk_bf16(q[2], q[3]);
;                 *(u32x2*)(zp + dd * 32 + 8 * g) = wp; *(u32x2*)(zp + 512 + dd * 32 + 8 * g) = wq;
;             }
	v_pk_mul_f32 v[2:3], v[20:21], v[218:219]
	v_mov_b32_e32 v4, v21
	v_sub_f32_e32 v20, v2, v3
	v_pk_mul_f32 v[2:3], v[4:5], v[218:219]
	s_nop 0
	v_add_f32_e32 v5, v3, v2
	v_cvt_pk_bf16_f32 v2, v36, v18
	v_cvt_pk_bf16_f32 v3, v34, v20
	v_cvt_pk_bf16_f32 v4, v37, v19
	v_cvt_pk_bf16_f32 v5, v35, v5
	ds_write_b64 v176, v[2:3] offset:64
	ds_write_b64 v176, v[4:5] offset:192
	v_mov_b32_e32 v2, v6
	v_mov_b32_e32 v3, v22
	v_pk_mul_f32 v[2:3], v[2:3], v[218:219]
	s_nop 0
	v_sub_f32_e32 v4, v2, v3
	v_mov_b32_e32 v2, v22
	v_mov_b32_e32 v3, v6
	v_pk_mul_f32 v[2:3], v[2:3], v[218:219]
	v_mov_b32_e32 v22, v7
	v_add_f32_e32 v5, v3, v2
	v_pk_mul_f32 v[2:3], v[22:23], v[218:219]
	v_mov_b32_e32 v6, v23
	v_sub_f32_e32 v18, v2, v3
	v_pk_mul_f32 v[2:3], v[6:7], v[218:219]
	s_nop 0
	v_add_f32_e32 v6, v3, v2
	v_mov_b32_e32 v2, v8
	v_mov_b32_e32 v3, v24
	v_pk_mul_f32 v[2:3], v[2:3], v[218:219]
	s_nop 0
	v_sub_f32_e32 v7, v2, v3
	v_mov_b32_e32 v2, v24
	v_mov_b32_e32 v3, v8
	v_pk_mul_f32 v[2:3], v[2:3], v[218:219]
	v_mov_b32_e32 v24, v9
	v_add_f32_e32 v19, v3, v2
	v_pk_mul_f32 v[2:3], v[24:25], v[218:219]
	v_mov_b32_e32 v8, v25
	v_sub_f32_e32 v20, v2, v3
	v_pk_mul_f32 v[2:3], v[8:9], v[218:219]
	s_nop 0
	v_add_f32_e32 v8, v3, v2
	v_cvt_pk_bf16_f32 v2, v4, v18
	v_cvt_pk_bf16_f32 v3, v7, v20
	v_cvt_pk_bf16_f32 v4, v5, v6
	v_cvt_pk_bf16_f32 v5, v19, v8
	ds_write_b64 v176, v[2:3] offset:80
	ds_write_b64 v176, v[4:5] offset:208
	v_mov_b32_e32 v2, v10
	v_mov_b32_e32 v3, v26
	v_pk_mul_f32 v[2:3], v[2:3], v[218:219]
	s_nop 0
	v_sub_f32_e32 v4, v2, v3
	v_mov_b32_e32 v2, v26
	v_mov_b32_e32 v3, v10
	v_pk_mul_f32 v[2:3], v[2:3], v[218:219]
	v_mov_b32_e32 v26, v11
	v_add_f32_e32 v5, v3, v2
	v_pk_mul_f32 v[2:3], v[26:27], v[218:219]
	v_mov_b32_e32 v10, v27
	v_sub_f32_e32 v6, v2, v3
	v_pk_mul_f32 v[2:3], v[10:11], v[218:219]
	s_nop 0
	v_add_f32_e32 v7, v3, v2
	v_mov_b32_e32 v2, v12
	v_mov_b32_e32 v3, v28
	v_pk_mul_f32 v[2:3], v[2:3], v[218:219]
	s_nop 0
	v_sub_f32_e32 v8, v2, v3
	v_mov_b32_e32 v2, v28
	v_mov_b32_e32 v3, v12
	v_pk_mul_f32 v[2:3], v[2:3], v[218:219]
	v_mov_b32_e32 v28, v13
	v_add_f32_e32 v9, v3, v2
	v_pk_mul_f32 v[2:3], v[28:29], v[218:219]
	v_mov_b32_e32 v12, v29
	v_sub_f32_e32 v10, v2, v3
	v_pk_mul_f32 v[2:3], v[12:13], v[218:219]
	s_nop 0
	v_add_f32_e32 v11, v3, v2
	v_cvt_pk_bf16_f32 v2, v4, v6
	v_cvt_pk_bf16_f32 v3, v8, v10
	v_cvt_pk_bf16_f32 v4, v5, v7
	v_cvt_pk_bf16_f32 v5, v9, v11
	ds_write_b64 v176, v[2:3] offset:96
	ds_write_b64 v176, v[4:5] offset:224
	v_mov_b32_e32 v2, v14
	v_mov_b32_e32 v3, v30
	v_pk_mul_f32 v[2:3], v[2:3], v[218:219]
	s_nop 0
	v_sub_f32_e32 v4, v2, v3
	v_mov_b32_e32 v2, v30
	v_mov_b32_e32 v3, v14
	v_pk_mul_f32 v[2:3], v[2:3], v[218:219]
	v_mov_b32_e32 v30, v15
	v_add_f32_e32 v5, v3, v2
	v_pk_mul_f32 v[2:3], v[30:31], v[218:219]
	v_mov_b32_e32 v14, v31
	v_sub_f32_e32 v6, v2, v3
	v_pk_mul_f32 v[2:3], v[14:15], v[218:219]
	s_nop 0
	v_add_f32_e32 v7, v3, v2
	v_mov_b32_e32 v2, v16
	v_mov_b32_e32 v3, v32
	v_pk_mul_f32 v[2:3], v[2:3], v[218:219]
	s_nop 0
	v_sub_f32_e32 v8, v2, v3
	v_mov_b32_e32 v2, v32
	v_mov_b32_e32 v3, v16
	v_pk_mul_f32 v[2:3], v[2:3], v[218:219]
	v_mov_b32_e32 v32, v17
	v_add_f32_e32 v9, v3, v2
	v_pk_mul_f32 v[2:3], v[32:33], v[218:219]
	v_mov_b32_e32 v16, v33
	v_sub_f32_e32 v10, v2, v3
	v_pk_mul_f32 v[2:3], v[16:17], v[218:219]
	s_nop 0
	v_add_f32_e32 v11, v3, v2
	v_cvt_pk_bf16_f32 v2, v4, v6
	v_cvt_pk_bf16_f32 v3, v8, v10
	v_cvt_pk_bf16_f32 v4, v5, v7
	v_cvt_pk_bf16_f32 v5, v9, v11
	ds_write_b64 v176, v[2:3] offset:112
	ds_write_b64 v176, v[4:5] offset:240
	s_waitcnt lgkmcnt(0)
	ds_read_b128 v[184:187], v177
	ds_read_b128 v[188:191], v177 offset:2176
	ds_read_b128 v[192:195], v177 offset:4352
	ds_read_b128 v[198:201], v177 offset:6528
	ds_read_b128 v[202:205], v177 offset:128
	ds_read_b128 v[206:209], v177 offset:2304
	ds_read_b128 v[210:213], v177 offset:4480
	ds_read_b128 v[214:217], v177 offset:6656
	s_mov_b64 s[100:101], 0x100000
	v_lshl_add_u64 v[178:179], v[118:119], 0, s[100:101]
	v_lshl_add_u64 v[180:181], v[178:179], 0, s[100:101]
	v_lshl_add_u64 v[182:183], v[180:181], 0, s[100:101]
	s_waitcnt lgkmcnt(7)
	global_store_dwordx4 v[118:119], v[184:187], off
	s_waitcnt lgkmcnt(6)
	global_store_dwordx4 v[178:179], v[188:191], off
	s_waitcnt lgkmcnt(5)
	global_store_dwordx4 v[180:181], v[192:195], off
	s_waitcnt lgkmcnt(4)
	global_store_dwordx4 v[182:183], v[198:201], off
	s_waitcnt lgkmcnt(3)
	global_store_dwordx4 v[118:119], v[202:205], off offset:1024
	s_waitcnt lgkmcnt(2)
	global_store_dwordx4 v[178:179], v[206:209], off offset:1024
	s_waitcnt lgkmcnt(1)
	global_store_dwordx4 v[180:181], v[210:213], off offset:1024
	s_waitcnt lgkmcnt(0)
	global_store_dwordx4 v[182:183], v[214:217], off offset:1024
	s_cbranch_vccz .LBB0_331

;     __device__ __forceinline__ float* tw() const { return (float*)(ws + WS_TW); }
; __device__ __forceinline__ int v_rd_base(int lane) { return ((lane & 3) << 3) | (((lane >> 2) & 3) << 6) | (((lane >> 4) & 1) << 5) | (((lane >> 5) & 1) << 8); }
; __device__ __forceinline__ void phase_fft_a(const Frame& F) {
;     ...
;             for (int ks = 0; ks < 4; ++ks) { const int o = k1 * 128 + t * 64 + ks * 16 + hi * 8; bc[ks] = *(const bf16x8*)(dc + o); bs[ks] = *(const bf16x8*)(ds + o); }
;             const int vb = (int)(uintptr_t)img + t * 16384 + ff::v_rd_base(lane) + chh * 1024;
;             ff::xt_two<0>(zc[0], zs[0], vb, bc, bs);
;             ff::xt_two<1>(zc[1], zs[1], vb, bc, bs);
;         }
;         const f32x2 t2 = *(const f32x2*)(F.tw() + (size_t)(k1 * 64 + n2) * 2);
.LBB0_329:
	s_bfe_u32 s100, s23, 0x60002
	global_load_dwordx4 v[2:5], v[82:83], off
	global_load_dwordx4 v[18:21], v[84:85], off
	global_load_dwordx4 v[116:119], v[86:87], off
	global_load_dwordx4 v[128:131], v[88:89], off
	global_load_dwordx4 v[132:135], v[90:91], off
	global_load_dwordx4 v[136:139], v[92:93], off
	global_load_dwordx4 v[140:143], v[94:95], off
	global_load_dwordx4 v[148:151], v[96:97], off
	global_load_dwordx4 v[184:187], v[98:99], off
	global_load_dwordx4 v[188:191], v[100:101], off
	global_load_dwordx4 v[192:195], v[102:103], off
	global_load_dwordx4 v[198:201], v[104:105], off
	global_load_dwordx4 v[202:205], v[106:107], off
	global_load_dwordx4 v[206:209], v[108:109], off
	global_load_dwordx4 v[210:213], v[110:111], off
	global_load_dwordx4 v[214:217], v[112:113], off
	v_lshl_or_b32 v218, s100, 3, v126
	global_load_dwordx2 v[218:219], v218, s[40:41]
	s_andn2_b64 vcc, exec, s[8:9]
	s_cbranch_vccnz .Lfa_nopf
	s_and_b32 s8, s1, 0xffffe000
	s_lshr_b32 s7, s2, 2
	v_add_u32_e32 v238, s8, v1
	v_and_or_b32 v238, s7, 63, v238
	v_readlane_b32 s7, v254, 4
	s_add_i32 s7, s7, s22
	v_ashrrev_i32_e32 v239, 31, v238
	s_and_b32 s8, s7, 0x180
	v_lshlrev_b64 v[240:241], 13, v[238:239]
	v_add_u32_e32 v242, 0x800, v238
	v_lshl_add_u64 v[240:241], s[56:57], 0, v[240:241]
	s_lshl_b32 s76, s8, 1
	v_ashrrev_i32_e32 v243, 31, v242
	v_lshl_add_u64 v[240:241], v[240:241], 0, s[76:77]
	v_mov_b32_e32 v115, v147
	v_lshlrev_b64 v[242:243], 13, v[242:243]
	v_lshl_add_u64 v[240:241], v[240:241], 0, v[114:115]
	s_mov_b32 s8, 0x1c317000
	v_lshl_add_u64 v[242:243], s[56:57], 0, v[242:243]
	v_add_co_u32_e32 v240, vcc, s8, v240
	v_lshl_add_u64 v[242:243], v[242:243], 0, s[76:77]
	s_nop 0
	v_addc_co_u32_e32 v241, vcc, 0, v241, vcc
	v_lshl_add_u64 v[242:243], v[242:243], 0, v[114:115]
	v_add_co_u32_e32 v242, vcc, s8, v242
	s_nop 1
	v_addc_co_u32_e32 v243, vcc, 0, v243, vcc
	global_load_dwordx4 v[66:69], v[240:241], off offset:2304
	global_load_dwordx4 v[70:73], v[242:243], off offset:2304
	v_add_u32_e32 v240, 0x1000, v238
	v_ashrrev_i32_e32 v241, 31, v240
	v_lshlrev_b64 v[240:241], 13, v[240:241]
	v_add_u32_e32 v238, 0x1800, v238
	v_lshl_add_u64 v[240:241], s[56:57], 0, v[240:241]
	v_ashrrev_i32_e32 v239, 31, v238
	v_lshl_add_u64 v[240:241], v[240:241], 0, s[76:77]
	v_lshlrev_b64 v[238:239], 13, v[238:239]
	v_lshl_add_u64 v[240:241], v[240:241], 0, v[114:115]
	v_lshl_add_u64 v[238:239], s[56:57], 0, v[238:239]
	v_add_co_u32_e32 v240, vcc, s8, v240
	v_lshl_add_u64 v[238:239], v[238:239], 0, s[76:77]
	s_nop 0
	v_addc_co_u32_e32 v241, vcc, 0, v241, vcc
	v_lshl_add_u64 v[238:239], v[238:239], 0, v[114:115]
	v_add_co_u32_e32 v238, vcc, 0x1c317000, v238
	s_nop 1
	v_addc_co_u32_e32 v239, vcc, 0, v239, vcc
	global_load_dwordx4 v[74:77], v[240:241], off offset:2304
	global_load_dwordx4 v[78:81], v[238:239], off offset:2304
	s_branch .LBB0_326
